# P8/P11 epilogues: row sum-of-squares folded with v_permlane16_swap / v_permlane32_swap instead of ds_bpermute + lgkmcnt waits
# speedup vs baseline: 1.0043x; 1.0043x over previous
.LBB0_1121:
	s_lshl_b32 s4, s63, 8
	v_mov_b32_e32 v108, v0
	s_add_i32 s4, s4, s58
	v_and_b32_e32 v198, 64, v250
	v_and_or_b32 v216, v108, 15, s4
	s_lshl_b32 s4, s56, 8
	v_bfe_u32 v196, v108, 4, 2
	s_or_b32 s4, s4, s59
	v_lshl_or_b32 v214, v196, 3, s4
	v_ashrrev_i32_e32 v215, 31, v214
	v_ashrrev_i32_e32 v217, 31, v216
	v_lshlrev_b64 v[232:233], 1, v[214:215]
	v_lshl_add_u64 v[118:119], s[14:15], 0, v[232:233]
	v_lshlrev_b64 v[234:235], 11, v[216:217]
	v_lshl_add_u64 v[128:129], v[118:119], 0, v[234:235]
	global_load_dwordx4 v[192:195], v[128:129], off
	global_load_dwordx4 v[188:191], v[128:129], off offset:256
	v_or_b32_e32 v228, 16, v216
	v_ashrrev_i32_e32 v229, 31, v228
	v_or_b32_e32 v224, 32, v216
	v_ashrrev_i32_e32 v225, 31, v224
	v_or_b32_e32 v220, 48, v216
	v_lshlrev_b64 v[230:231], 11, v[228:229]
	v_ashrrev_i32_e32 v221, 31, v220
	v_lshl_add_u64 v[128:129], v[118:119], 0, v[230:231]
	v_lshlrev_b64 v[226:227], 11, v[224:225]
	v_add_u32_e32 v218, 0x80, v216
	v_add_u32_e32 v108, 0x90, v216
	global_load_dwordx4 v[184:187], v[128:129], off
	global_load_dwordx4 v[180:183], v[128:129], off offset:256
	v_lshl_add_u64 v[128:129], v[118:119], 0, v[226:227]
	v_lshlrev_b64 v[222:223], 11, v[220:221]
	v_ashrrev_i32_e32 v219, 31, v218
	v_ashrrev_i32_e32 v109, 31, v108
	global_load_dwordx4 v[176:179], v[128:129], off
	global_load_dwordx4 v[172:175], v[128:129], off offset:256
	v_lshl_add_u64 v[128:129], v[118:119], 0, v[222:223]
	v_add_u32_e32 v110, 0xa0, v216
	global_load_dwordx4 v[168:171], v[128:129], off
	global_load_dwordx4 v[164:167], v[128:129], off offset:256
	v_lshlrev_b64 v[128:129], 11, v[218:219]
	v_lshlrev_b64 v[108:109], 11, v[108:109]
	v_ashrrev_i32_e32 v111, 31, v110
	v_lshl_add_u64 v[128:129], v[118:119], 0, v[128:129]
	v_lshl_add_u64 v[108:109], v[118:119], 0, v[108:109]
	v_add_u32_e32 v116, 0xb0, v216
	global_load_dwordx4 v[160:163], v[128:129], off
	global_load_dwordx4 v[156:159], v[128:129], off offset:256
	global_load_dwordx4 v[152:155], v[108:109], off
	global_load_dwordx4 v[148:151], v[108:109], off offset:256
	v_lshlrev_b64 v[108:109], 11, v[110:111]
	v_ashrrev_i32_e32 v117, 31, v116
	v_lshl_add_u64 v[108:109], v[118:119], 0, v[108:109]
	global_load_dwordx4 v[136:139], v[108:109], off
	global_load_dwordx4 v[128:131], v[108:109], off offset:256
	v_lshlrev_b64 v[108:109], 11, v[116:117]
	v_lshl_add_u64 v[108:109], v[118:119], 0, v[108:109]
	global_load_dwordx4 v[116:119], v[108:109], off
	s_nop 0
	global_load_dwordx4 v[108:111], v[108:109], off offset:256
	v_xor_b32_e32 v197, 16, v250
	v_add_u32_e32 v198, 64, v198
	v_cmp_lt_i32_e32 vcc, v197, v198
	s_lshl_b32 s44, s56, 2
	s_ashr_i32 s45, s44, 31
	v_cndmask_b32_e32 v197, v250, v197, vcc
	v_lshlrev_b32_e32 v237, 2, v197
	v_xor_b32_e32 v197, 32, v250
	v_cmp_lt_i32_e32 vcc, v197, v198
	s_waitcnt vmcnt(0)
	v_lshlrev_b32_e32 v198, 16, v194
	v_cndmask_b32_e32 v197, v250, v197, vcc
	v_lshlrev_b32_e32 v238, 2, v197
	v_cmp_eq_u32_e32 vcc, 0, v196
	v_lshlrev_b32_e32 v196, 16, v192
	v_and_b32_e32 v197, 0xffff0000, v192
	v_lshlrev_b32_e32 v192, 16, v193
	v_and_b32_e32 v193, 0xffff0000, v193
	v_and_b32_e32 v199, 0xffff0000, v194
	v_lshlrev_b32_e32 v194, 16, v195
	v_and_b32_e32 v195, 0xffff0000, v195
	v_pk_add_f32 v[144:145], v[144:145], v[196:197]
	v_pk_add_f32 v[146:147], v[146:147], v[192:193]
	v_pk_add_f32 v[192:193], v[142:143], v[194:195]
	v_pk_add_f32 v[142:143], v[140:141], v[198:199]
	v_cvt_pk_bf16_f32 v140, v144, v145
	v_lshl_add_u64 v[144:145], s[14:15], 0, v[234:235]
	v_cvt_pk_bf16_f32 v141, v146, v147
	v_cvt_pk_bf16_f32 v142, v142, v143
	v_cvt_pk_bf16_f32 v143, v192, v193
	v_lshl_add_u64 v[144:145], v[144:145], 0, v[232:233]
	global_store_dwordx4 v[144:145], v[140:143], off
	v_lshlrev_b32_e32 v146, 16, v140
	v_lshlrev_b32_e32 v147, 16, v141
	v_and_b32_e32 v140, 0xffff0000, v140
	v_and_b32_e32 v141, 0xffff0000, v141
	v_mul_f32_e32 v140, v140, v140
	v_mul_f32_e32 v141, v141, v141
	v_lshlrev_b32_e32 v192, 16, v142
	v_and_b32_e32 v142, 0xffff0000, v142
	v_lshlrev_b32_e32 v193, 16, v143
	v_and_b32_e32 v143, 0xffff0000, v143
	v_fmac_f32_e32 v140, v146, v146
	v_fmac_f32_e32 v141, v147, v147
	v_add_f32_e32 v140, v140, v141
	v_mul_f32_e32 v141, v142, v142
	v_mul_f32_e32 v142, v143, v143
	v_fmac_f32_e32 v141, v192, v192
	v_fmac_f32_e32 v142, v193, v193
	v_add_f32_e32 v141, v141, v142
	v_add_f32_e32 v192, v140, v141
	v_lshlrev_b32_e32 v140, 16, v188
	v_and_b32_e32 v141, 0xffff0000, v188
	v_lshlrev_b32_e32 v142, 16, v189
	v_and_b32_e32 v143, 0xffff0000, v189
	v_lshlrev_b32_e32 v146, 16, v190
	v_and_b32_e32 v147, 0xffff0000, v190
	v_lshlrev_b32_e32 v188, 16, v191
	v_and_b32_e32 v189, 0xffff0000, v191
	v_pk_add_f32 v[134:135], v[134:135], v[142:143]
	v_pk_add_f32 v[132:133], v[132:133], v[140:141]
	v_pk_add_f32 v[140:141], v[126:127], v[188:189]
	v_pk_add_f32 v[126:127], v[124:125], v[146:147]
	v_cvt_pk_bf16_f32 v124, v132, v133
	v_cvt_pk_bf16_f32 v125, v134, v135
	v_cvt_pk_bf16_f32 v126, v126, v127
	v_cvt_pk_bf16_f32 v127, v140, v141
	global_store_dwordx4 v[144:145], v[124:127], off offset:256
	v_lshlrev_b32_e32 v132, 16, v124
	v_lshlrev_b32_e32 v133, 16, v125
	v_and_b32_e32 v124, 0xffff0000, v124
	v_and_b32_e32 v125, 0xffff0000, v125
	v_mul_f32_e32 v124, v124, v124
	v_mul_f32_e32 v125, v125, v125
	v_lshlrev_b32_e32 v134, 16, v126
	v_and_b32_e32 v126, 0xffff0000, v126
	v_lshlrev_b32_e32 v135, 16, v127
	v_and_b32_e32 v127, 0xffff0000, v127
	v_fmac_f32_e32 v124, v132, v132
	v_fmac_f32_e32 v125, v133, v133
	v_add_f32_e32 v124, v124, v125
	v_mul_f32_e32 v125, v126, v126
	v_mul_f32_e32 v126, v127, v127
	v_fmac_f32_e32 v125, v134, v134
	v_fmac_f32_e32 v126, v135, v135
	v_add_f32_e32 v125, v125, v126
	v_add_f32_e32 v124, v124, v125
	v_add_f32_e32 v124, v192, v124
	v_mov_b32_e32 v125, v124
	s_nop 3
	v_permlane16_swap_b32_e32 v124, v125
	s_nop 1
	s_waitcnt lgkmcnt(0)
	v_add_f32_e32 v124, v124, v125
	v_mov_b32_e32 v125, v124
	s_nop 3
	v_permlane32_swap_b32_e32 v124, v125
	s_nop 1
	s_and_saveexec_b64 s[4:5], vcc
	s_cbranch_execz .LBB0_1123
	v_lshlrev_b64 v[126:127], 6, v[216:217]
	v_lshl_add_u64 v[126:127], s[18:19], 0, v[126:127]
	v_lshl_add_u64 v[126:127], s[44:45], 2, v[126:127]
	s_lshl_b32 s56, s53, 2
	v_lshl_add_u64 v[126:127], v[126:127], 0, s[56:57]
	s_waitcnt lgkmcnt(0)
	v_add_f32_e32 v124, v124, v125
	global_store_dword v[126:127], v124, off
.LBB0_1123:
	s_or_b64 exec, exec, s[4:5]
	v_lshlrev_b32_e32 v124, 16, v184
	s_waitcnt lgkmcnt(0)
	v_and_b32_e32 v125, 0xffff0000, v184
	v_lshlrev_b32_e32 v126, 16, v185
	v_and_b32_e32 v127, 0xffff0000, v185
	v_lshlrev_b32_e32 v132, 16, v186
	v_and_b32_e32 v133, 0xffff0000, v186
	v_lshlrev_b32_e32 v134, 16, v187
	v_and_b32_e32 v135, 0xffff0000, v187
	v_pk_add_f32 v[120:121], v[120:121], v[124:125]
	v_pk_add_f32 v[122:123], v[122:123], v[126:127]
	v_pk_add_f32 v[124:125], v[114:115], v[134:135]
	v_pk_add_f32 v[114:115], v[112:113], v[132:133]
	v_cvt_pk_bf16_f32 v112, v120, v121
	v_cvt_pk_bf16_f32 v113, v122, v123
	v_and_b32_e32 v121, 0xffff0000, v112
	v_lshlrev_b32_e32 v120, 16, v112
	v_and_b32_e32 v123, 0xffff0000, v113
	v_mul_f32_e32 v121, v121, v121
	v_cvt_pk_bf16_f32 v114, v114, v115
	v_cvt_pk_bf16_f32 v115, v124, v125
	v_lshlrev_b32_e32 v122, 16, v113
	v_fmac_f32_e32 v121, v120, v120
	v_mul_f32_e32 v120, v123, v123
	v_and_b32_e32 v125, 0xffff0000, v114
	v_and_b32_e32 v127, 0xffff0000, v115
	v_fmac_f32_e32 v120, v122, v122
	v_lshlrev_b32_e32 v124, 16, v114
	v_lshlrev_b32_e32 v126, 16, v115
	v_add_f32_e32 v120, v121, v120
	v_mul_f32_e32 v121, v125, v125
	v_mul_f32_e32 v122, v127, v127
	v_fmac_f32_e32 v121, v124, v124
	v_fmac_f32_e32 v122, v126, v126
	v_add_f32_e32 v121, v121, v122
	v_add_f32_e32 v132, v120, v121
	v_lshlrev_b32_e32 v120, 16, v180
	v_and_b32_e32 v121, 0xffff0000, v180
	v_lshlrev_b32_e32 v122, 16, v181
	v_and_b32_e32 v123, 0xffff0000, v181
	v_lshlrev_b32_e32 v124, 16, v182
	v_and_b32_e32 v125, 0xffff0000, v182
	v_lshlrev_b32_e32 v126, 16, v183
	v_and_b32_e32 v127, 0xffff0000, v183
	v_pk_add_f32 v[104:105], v[104:105], v[120:121]
	v_pk_add_f32 v[106:107], v[106:107], v[122:123]
	v_pk_add_f32 v[120:121], v[102:103], v[126:127]
	v_pk_add_f32 v[100:101], v[100:101], v[124:125]
	v_cvt_pk_bf16_f32 v102, v104, v105
	v_cvt_pk_bf16_f32 v103, v106, v107
	v_cvt_pk_bf16_f32 v104, v100, v101
	v_and_b32_e32 v101, 0xffff0000, v102
	v_lshlrev_b32_e32 v100, 16, v102
	v_and_b32_e32 v107, 0xffff0000, v103
	v_mul_f32_e32 v101, v101, v101
	v_cvt_pk_bf16_f32 v105, v120, v121
	v_lshlrev_b32_e32 v106, 16, v103
	v_fmac_f32_e32 v101, v100, v100
	v_mul_f32_e32 v100, v107, v107
	v_and_b32_e32 v121, 0xffff0000, v104
	v_and_b32_e32 v123, 0xffff0000, v105
	v_fmac_f32_e32 v100, v106, v106
	v_lshlrev_b32_e32 v120, 16, v104
	v_lshlrev_b32_e32 v122, 16, v105
	v_add_f32_e32 v100, v101, v100
	v_mul_f32_e32 v101, v121, v121
	v_mul_f32_e32 v106, v123, v123
	v_fmac_f32_e32 v101, v120, v120
	v_fmac_f32_e32 v106, v122, v122
	v_add_f32_e32 v101, v101, v106
	v_add_f32_e32 v100, v100, v101
	v_add_f32_e32 v100, v132, v100
	v_mov_b32_e32 v101, v100
	s_nop 3
	v_permlane16_swap_b32_e32 v100, v101
	s_nop 1
	v_lshl_add_u64 v[106:107], s[14:15], 0, v[230:231]
	v_lshl_add_u64 v[106:107], v[214:215], 1, v[106:107]
	global_store_dwordx4 v[106:107], v[112:115], off
	global_store_dwordx4 v[106:107], v[102:105], off offset:256
	s_waitcnt lgkmcnt(0)
	v_add_f32_e32 v100, v100, v101
	v_mov_b32_e32 v101, v100
	s_nop 3
	v_permlane32_swap_b32_e32 v100, v101
	s_nop 1
	s_and_saveexec_b64 s[4:5], vcc
	s_cbranch_execz .LBB0_1125
	v_lshlrev_b64 v[102:103], 6, v[228:229]
	v_lshl_add_u64 v[102:103], s[18:19], 0, v[102:103]
	v_lshl_add_u64 v[102:103], s[44:45], 2, v[102:103]
	s_lshl_b32 s56, s53, 2
	v_lshl_add_u64 v[102:103], v[102:103], 0, s[56:57]
	s_waitcnt lgkmcnt(0)
	v_add_f32_e32 v100, v100, v101
	global_store_dword v[102:103], v100, off
.LBB0_1125:
	s_or_b64 exec, exec, s[4:5]
	v_lshlrev_b32_e32 v100, 16, v176
	s_waitcnt lgkmcnt(0)
	v_and_b32_e32 v101, 0xffff0000, v176
	v_lshlrev_b32_e32 v102, 16, v177
	v_and_b32_e32 v103, 0xffff0000, v177
	v_lshlrev_b32_e32 v104, 16, v178
	v_and_b32_e32 v105, 0xffff0000, v178
	v_lshlrev_b32_e32 v106, 16, v179
	v_and_b32_e32 v107, 0xffff0000, v179
	v_pk_add_f32 v[96:97], v[96:97], v[100:101]
	v_pk_add_f32 v[98:99], v[98:99], v[102:103]
	v_pk_add_f32 v[100:101], v[94:95], v[106:107]
	v_pk_add_f32 v[94:95], v[92:93], v[104:105]
	v_cvt_pk_bf16_f32 v92, v96, v97
	v_cvt_pk_bf16_f32 v93, v98, v99
	v_and_b32_e32 v97, 0xffff0000, v92
	v_lshlrev_b32_e32 v96, 16, v92
	v_and_b32_e32 v99, 0xffff0000, v93
	v_mul_f32_e32 v97, v97, v97
	v_cvt_pk_bf16_f32 v94, v94, v95
	v_cvt_pk_bf16_f32 v95, v100, v101
	v_lshlrev_b32_e32 v98, 16, v93
	v_fmac_f32_e32 v97, v96, v96
	v_mul_f32_e32 v96, v99, v99
	v_and_b32_e32 v101, 0xffff0000, v94
	v_and_b32_e32 v103, 0xffff0000, v95
	v_fmac_f32_e32 v96, v98, v98
	v_lshlrev_b32_e32 v100, 16, v94
	v_lshlrev_b32_e32 v102, 16, v95
	v_add_f32_e32 v96, v97, v96
	v_mul_f32_e32 v97, v101, v101
	v_mul_f32_e32 v98, v103, v103
	v_fmac_f32_e32 v97, v100, v100
	v_fmac_f32_e32 v98, v102, v102
	v_add_f32_e32 v97, v97, v98
	v_add_f32_e32 v104, v96, v97
	v_lshlrev_b32_e32 v96, 16, v172
	v_and_b32_e32 v97, 0xffff0000, v172
	v_lshlrev_b32_e32 v98, 16, v173
	v_and_b32_e32 v99, 0xffff0000, v173
	v_lshlrev_b32_e32 v100, 16, v174
	v_and_b32_e32 v101, 0xffff0000, v174
	v_lshlrev_b32_e32 v102, 16, v175
	v_and_b32_e32 v103, 0xffff0000, v175
	v_pk_add_f32 v[88:89], v[88:89], v[96:97]
	v_pk_add_f32 v[90:91], v[90:91], v[98:99]
	v_pk_add_f32 v[96:97], v[86:87], v[102:103]
	v_pk_add_f32 v[84:85], v[84:85], v[100:101]
	v_cvt_pk_bf16_f32 v86, v88, v89
	v_cvt_pk_bf16_f32 v87, v90, v91
	v_cvt_pk_bf16_f32 v88, v84, v85
	v_and_b32_e32 v85, 0xffff0000, v86
	v_lshlrev_b32_e32 v84, 16, v86
	v_and_b32_e32 v91, 0xffff0000, v87
	v_mul_f32_e32 v85, v85, v85
	v_cvt_pk_bf16_f32 v89, v96, v97
	v_lshlrev_b32_e32 v90, 16, v87
	v_fmac_f32_e32 v85, v84, v84
	v_mul_f32_e32 v84, v91, v91
	v_and_b32_e32 v97, 0xffff0000, v88
	v_and_b32_e32 v99, 0xffff0000, v89
	v_fmac_f32_e32 v84, v90, v90
	v_lshlrev_b32_e32 v96, 16, v88
	v_lshlrev_b32_e32 v98, 16, v89
	v_add_f32_e32 v84, v85, v84
	v_mul_f32_e32 v85, v97, v97
	v_mul_f32_e32 v90, v99, v99
	v_fmac_f32_e32 v85, v96, v96
	v_fmac_f32_e32 v90, v98, v98
	v_add_f32_e32 v85, v85, v90
	v_add_f32_e32 v84, v84, v85
	v_add_f32_e32 v84, v104, v84
	v_mov_b32_e32 v85, v84
	s_nop 3
	v_permlane16_swap_b32_e32 v84, v85
	s_nop 1
	v_lshl_add_u64 v[90:91], s[14:15], 0, v[226:227]
	v_lshl_add_u64 v[90:91], v[214:215], 1, v[90:91]
	global_store_dwordx4 v[90:91], v[92:95], off
	global_store_dwordx4 v[90:91], v[86:89], off offset:256
	s_waitcnt lgkmcnt(0)
	v_add_f32_e32 v84, v84, v85
	v_mov_b32_e32 v85, v84
	s_nop 3
	v_permlane32_swap_b32_e32 v84, v85
	s_nop 1
	s_and_saveexec_b64 s[4:5], vcc
	s_mov_b32 s76, 0xe000
	s_movk_i32 s75, 0x3400
	v_readlane_b32 s74, v255, 38
	s_cbranch_execz .LBB0_1127
	v_lshlrev_b64 v[86:87], 6, v[224:225]
	v_lshl_add_u64 v[86:87], s[18:19], 0, v[86:87]
	v_lshl_add_u64 v[86:87], s[44:45], 2, v[86:87]
	s_lshl_b32 s56, s53, 2
	v_lshl_add_u64 v[86:87], v[86:87], 0, s[56:57]
	s_waitcnt lgkmcnt(0)
	v_add_f32_e32 v84, v84, v85
	global_store_dword v[86:87], v84, off
.LBB0_1127:
	s_or_b64 exec, exec, s[4:5]
	v_lshlrev_b32_e32 v84, 16, v168
	s_waitcnt lgkmcnt(0)
	v_and_b32_e32 v85, 0xffff0000, v168
	v_lshlrev_b32_e32 v86, 16, v169
	v_and_b32_e32 v87, 0xffff0000, v169
	v_lshlrev_b32_e32 v88, 16, v170
	v_and_b32_e32 v89, 0xffff0000, v170
	v_lshlrev_b32_e32 v90, 16, v171
	v_and_b32_e32 v91, 0xffff0000, v171
	v_pk_add_f32 v[80:81], v[80:81], v[84:85]
	v_pk_add_f32 v[82:83], v[82:83], v[86:87]
	v_pk_add_f32 v[84:85], v[78:79], v[90:91]
	v_pk_add_f32 v[78:79], v[76:77], v[88:89]
	v_cvt_pk_bf16_f32 v76, v80, v81
	v_cvt_pk_bf16_f32 v77, v82, v83
	v_and_b32_e32 v81, 0xffff0000, v76
	v_lshlrev_b32_e32 v80, 16, v76
	v_and_b32_e32 v83, 0xffff0000, v77
	v_mul_f32_e32 v81, v81, v81
	v_cvt_pk_bf16_f32 v78, v78, v79
	v_cvt_pk_bf16_f32 v79, v84, v85
	v_lshlrev_b32_e32 v82, 16, v77
	v_fmac_f32_e32 v81, v80, v80
	v_mul_f32_e32 v80, v83, v83
	v_and_b32_e32 v85, 0xffff0000, v78
	v_and_b32_e32 v87, 0xffff0000, v79
	v_fmac_f32_e32 v80, v82, v82
	v_lshlrev_b32_e32 v84, 16, v78
	v_lshlrev_b32_e32 v86, 16, v79
	v_add_f32_e32 v80, v81, v80
	v_mul_f32_e32 v81, v85, v85
	v_mul_f32_e32 v82, v87, v87
	v_fmac_f32_e32 v81, v84, v84
	v_fmac_f32_e32 v82, v86, v86
	v_add_f32_e32 v81, v81, v82
	v_add_f32_e32 v88, v80, v81
	v_lshlrev_b32_e32 v80, 16, v164
	v_and_b32_e32 v81, 0xffff0000, v164
	v_lshlrev_b32_e32 v82, 16, v165
	v_and_b32_e32 v83, 0xffff0000, v165
	v_lshlrev_b32_e32 v84, 16, v166
	v_and_b32_e32 v85, 0xffff0000, v166
	v_lshlrev_b32_e32 v86, 16, v167
	v_and_b32_e32 v87, 0xffff0000, v167
	v_pk_add_f32 v[72:73], v[72:73], v[80:81]
	v_pk_add_f32 v[74:75], v[74:75], v[82:83]
	v_pk_add_f32 v[80:81], v[70:71], v[86:87]
	v_pk_add_f32 v[68:69], v[68:69], v[84:85]
	v_cvt_pk_bf16_f32 v70, v72, v73
	v_cvt_pk_bf16_f32 v71, v74, v75
	v_cvt_pk_bf16_f32 v72, v68, v69
	v_and_b32_e32 v69, 0xffff0000, v70
	v_lshlrev_b32_e32 v68, 16, v70
	v_and_b32_e32 v75, 0xffff0000, v71
	v_mul_f32_e32 v69, v69, v69
	v_cvt_pk_bf16_f32 v73, v80, v81
	v_lshlrev_b32_e32 v74, 16, v71
	v_fmac_f32_e32 v69, v68, v68
	v_mul_f32_e32 v68, v75, v75
	v_and_b32_e32 v81, 0xffff0000, v72
	v_and_b32_e32 v83, 0xffff0000, v73
	v_fmac_f32_e32 v68, v74, v74
	v_lshlrev_b32_e32 v80, 16, v72
	v_lshlrev_b32_e32 v82, 16, v73
	v_add_f32_e32 v68, v69, v68
	v_mul_f32_e32 v69, v81, v81
	v_mul_f32_e32 v74, v83, v83
	v_fmac_f32_e32 v69, v80, v80
	v_fmac_f32_e32 v74, v82, v82
	v_add_f32_e32 v69, v69, v74
	v_add_f32_e32 v68, v68, v69
	v_add_f32_e32 v68, v88, v68
	v_mov_b32_e32 v69, v68
	s_nop 3
	v_permlane16_swap_b32_e32 v68, v69
	s_nop 1
	v_lshl_add_u64 v[74:75], s[14:15], 0, v[222:223]
	v_lshl_add_u64 v[74:75], v[214:215], 1, v[74:75]
	global_store_dwordx4 v[74:75], v[76:79], off
	global_store_dwordx4 v[74:75], v[70:73], off offset:256
	s_waitcnt lgkmcnt(0)
	v_add_f32_e32 v68, v68, v69
	v_mov_b32_e32 v69, v68
	s_nop 3
	v_permlane32_swap_b32_e32 v68, v69
	s_nop 1
	s_and_saveexec_b64 s[4:5], vcc
	s_cbranch_execz .LBB0_1129
	v_lshlrev_b64 v[70:71], 6, v[220:221]
	v_lshl_add_u64 v[70:71], s[18:19], 0, v[70:71]
	v_lshl_add_u64 v[70:71], s[44:45], 2, v[70:71]
	s_lshl_b32 s56, s53, 2
	v_lshl_add_u64 v[70:71], v[70:71], 0, s[56:57]
	s_waitcnt lgkmcnt(0)
	v_add_f32_e32 v68, v68, v69
	global_store_dword v[70:71], v68, off
.LBB0_1129:
	s_or_b64 exec, exec, s[4:5]
	v_lshlrev_b32_e32 v68, 16, v160
	s_waitcnt lgkmcnt(0)
	v_and_b32_e32 v69, 0xffff0000, v160
	v_lshlrev_b32_e32 v70, 16, v161
	v_and_b32_e32 v71, 0xffff0000, v161
	v_lshlrev_b32_e32 v72, 16, v162
	v_and_b32_e32 v73, 0xffff0000, v162
	v_lshlrev_b32_e32 v74, 16, v163
	v_and_b32_e32 v75, 0xffff0000, v163
	v_pk_add_f32 v[64:65], v[64:65], v[68:69]
	v_pk_add_f32 v[66:67], v[66:67], v[70:71]
	v_pk_add_f32 v[68:69], v[62:63], v[74:75]
	v_pk_add_f32 v[62:63], v[60:61], v[72:73]
	v_cvt_pk_bf16_f32 v60, v64, v65
	v_cvt_pk_bf16_f32 v61, v66, v67
	v_and_b32_e32 v65, 0xffff0000, v60
	v_lshlrev_b32_e32 v64, 16, v60
	v_and_b32_e32 v67, 0xffff0000, v61
	v_mul_f32_e32 v65, v65, v65
	v_cvt_pk_bf16_f32 v62, v62, v63
	v_cvt_pk_bf16_f32 v63, v68, v69
	v_lshlrev_b32_e32 v66, 16, v61
	v_fmac_f32_e32 v65, v64, v64
	v_mul_f32_e32 v64, v67, v67
	v_and_b32_e32 v69, 0xffff0000, v62
	v_and_b32_e32 v71, 0xffff0000, v63
	v_fmac_f32_e32 v64, v66, v66
	v_lshlrev_b32_e32 v68, 16, v62
	v_lshlrev_b32_e32 v70, 16, v63
	v_add_f32_e32 v64, v65, v64
	v_mul_f32_e32 v65, v69, v69
	v_mul_f32_e32 v66, v71, v71
	v_fmac_f32_e32 v65, v68, v68
	v_fmac_f32_e32 v66, v70, v70
	v_add_f32_e32 v65, v65, v66
	v_add_f32_e32 v72, v64, v65
	v_lshlrev_b32_e32 v64, 16, v156
	v_and_b32_e32 v65, 0xffff0000, v156
	v_lshlrev_b32_e32 v66, 16, v157
	v_and_b32_e32 v67, 0xffff0000, v157
	v_lshlrev_b32_e32 v68, 16, v158
	v_and_b32_e32 v69, 0xffff0000, v158
	v_lshlrev_b32_e32 v70, 16, v159
	v_and_b32_e32 v71, 0xffff0000, v159
	v_pk_add_f32 v[56:57], v[56:57], v[64:65]
	v_pk_add_f32 v[58:59], v[58:59], v[66:67]
	v_pk_add_f32 v[64:65], v[54:55], v[70:71]
	v_pk_add_f32 v[52:53], v[52:53], v[68:69]
	v_cvt_pk_bf16_f32 v54, v56, v57
	v_cvt_pk_bf16_f32 v55, v58, v59
	v_cvt_pk_bf16_f32 v56, v52, v53
	v_and_b32_e32 v53, 0xffff0000, v54
	v_lshlrev_b32_e32 v52, 16, v54
	v_and_b32_e32 v59, 0xffff0000, v55
	v_mul_f32_e32 v53, v53, v53
	v_cvt_pk_bf16_f32 v57, v64, v65
	v_lshlrev_b32_e32 v58, 16, v55
	v_fmac_f32_e32 v53, v52, v52
	v_mul_f32_e32 v52, v59, v59
	v_and_b32_e32 v65, 0xffff0000, v56
	v_and_b32_e32 v67, 0xffff0000, v57
	v_fmac_f32_e32 v52, v58, v58
	v_lshlrev_b32_e32 v64, 16, v56
	v_lshlrev_b32_e32 v66, 16, v57
	v_add_f32_e32 v52, v53, v52
	v_mul_f32_e32 v53, v65, v65
	v_mul_f32_e32 v58, v67, v67
	v_fmac_f32_e32 v53, v64, v64
	v_fmac_f32_e32 v58, v66, v66
	v_add_f32_e32 v53, v53, v58
	v_add_f32_e32 v52, v52, v53
	v_add_f32_e32 v52, v72, v52
	v_mov_b32_e32 v53, v52
	s_nop 3
	v_permlane16_swap_b32_e32 v52, v53
	s_nop 1
	v_lshlrev_b64 v[58:59], 10, v[218:219]
	v_lshl_add_u64 v[58:59], v[58:59], 1, s[14:15]
	v_lshl_add_u64 v[58:59], v[214:215], 1, v[58:59]
	global_store_dwordx4 v[58:59], v[60:63], off
	global_store_dwordx4 v[58:59], v[54:57], off offset:256
	s_waitcnt lgkmcnt(0)
	v_add_f32_e32 v52, v52, v53
	v_mov_b32_e32 v53, v52
	s_nop 3
	v_permlane32_swap_b32_e32 v52, v53
	s_nop 1
	s_and_saveexec_b64 s[4:5], vcc
	s_cbranch_execz .LBB0_1131
	v_lshlrev_b64 v[54:55], 6, v[218:219]
	v_lshl_add_u64 v[54:55], s[18:19], 0, v[54:55]
	v_lshl_add_u64 v[54:55], s[44:45], 2, v[54:55]
	s_lshl_b32 s56, s53, 2
	v_lshl_add_u64 v[54:55], v[54:55], 0, s[56:57]
	s_waitcnt lgkmcnt(0)
	v_add_f32_e32 v52, v52, v53
	global_store_dword v[54:55], v52, off
.LBB0_1131:
	s_or_b64 exec, exec, s[4:5]
	v_lshlrev_b32_e32 v52, 16, v152
	s_waitcnt lgkmcnt(0)
	v_and_b32_e32 v53, 0xffff0000, v152
	v_lshlrev_b32_e32 v54, 16, v153
	v_and_b32_e32 v55, 0xffff0000, v153
	v_lshlrev_b32_e32 v56, 16, v154
	v_and_b32_e32 v57, 0xffff0000, v154
	v_lshlrev_b32_e32 v58, 16, v155
	v_and_b32_e32 v59, 0xffff0000, v155
	v_pk_add_f32 v[48:49], v[48:49], v[52:53]
	v_pk_add_f32 v[50:51], v[50:51], v[54:55]
	v_pk_add_f32 v[52:53], v[46:47], v[58:59]
	v_pk_add_f32 v[46:47], v[44:45], v[56:57]
	v_cvt_pk_bf16_f32 v44, v48, v49
	v_cvt_pk_bf16_f32 v45, v50, v51
	v_and_b32_e32 v49, 0xffff0000, v44
	v_lshlrev_b32_e32 v48, 16, v44
	v_and_b32_e32 v51, 0xffff0000, v45
	v_mul_f32_e32 v49, v49, v49
	v_cvt_pk_bf16_f32 v46, v46, v47
	v_cvt_pk_bf16_f32 v47, v52, v53
	v_lshlrev_b32_e32 v50, 16, v45
	v_fmac_f32_e32 v49, v48, v48
	v_mul_f32_e32 v48, v51, v51
	v_and_b32_e32 v53, 0xffff0000, v46
	v_and_b32_e32 v55, 0xffff0000, v47
	v_fmac_f32_e32 v48, v50, v50
	v_lshlrev_b32_e32 v52, 16, v46
	v_lshlrev_b32_e32 v54, 16, v47
	v_add_f32_e32 v48, v49, v48
	v_mul_f32_e32 v49, v53, v53
	v_mul_f32_e32 v50, v55, v55
	v_fmac_f32_e32 v49, v52, v52
	v_fmac_f32_e32 v50, v54, v54
	v_add_f32_e32 v49, v49, v50
	v_add_f32_e32 v56, v48, v49
	v_lshlrev_b32_e32 v48, 16, v148
	v_and_b32_e32 v49, 0xffff0000, v148
	v_lshlrev_b32_e32 v50, 16, v149
	v_and_b32_e32 v51, 0xffff0000, v149
	v_lshlrev_b32_e32 v52, 16, v150
	v_and_b32_e32 v53, 0xffff0000, v150
	v_pk_add_f32 v[40:41], v[40:41], v[48:49]
	v_lshlrev_b32_e32 v54, 16, v151
	v_and_b32_e32 v55, 0xffff0000, v151
	v_pk_add_f32 v[42:43], v[42:43], v[50:51]
	v_pk_add_f32 v[36:37], v[36:37], v[52:53]
	v_cvt_pk_bf16_f32 v40, v40, v41
	v_pk_add_f32 v[38:39], v[38:39], v[54:55]
	v_cvt_pk_bf16_f32 v41, v42, v43
	v_cvt_pk_bf16_f32 v42, v36, v37
	v_and_b32_e32 v37, 0xffff0000, v40
	v_cvt_pk_bf16_f32 v43, v38, v39
	v_lshlrev_b32_e32 v36, 16, v40
	v_and_b32_e32 v39, 0xffff0000, v41
	v_mul_f32_e32 v37, v37, v37
	v_lshlrev_b32_e32 v38, 16, v41
	v_fmac_f32_e32 v37, v36, v36
	v_mul_f32_e32 v36, v39, v39
	v_and_b32_e32 v49, 0xffff0000, v42
	v_and_b32_e32 v51, 0xffff0000, v43
	v_fmac_f32_e32 v36, v38, v38
	v_lshlrev_b32_e32 v48, 16, v42
	v_lshlrev_b32_e32 v50, 16, v43
	v_add_f32_e32 v36, v37, v36
	v_mul_f32_e32 v37, v49, v49
	v_mul_f32_e32 v38, v51, v51
	v_fmac_f32_e32 v37, v48, v48
	v_fmac_f32_e32 v38, v50, v50
	v_add_f32_e32 v37, v37, v38
	v_add_f32_e32 v36, v36, v37
	v_add_f32_e32 v38, v56, v36
	v_mov_b32_e32 v39, v38
	s_nop 3
	v_permlane16_swap_b32_e32 v38, v39
	s_nop 1
	v_add_u32_e32 v36, 0x90, v216
	v_ashrrev_i32_e32 v37, 31, v36
	v_lshlrev_b64 v[48:49], 11, v[36:37]
	v_lshl_add_u64 v[48:49], s[14:15], 0, v[48:49]
	s_waitcnt lgkmcnt(0)
	v_add_f32_e32 v38, v38, v39
	v_mov_b32_e32 v39, v38
	s_nop 3
	v_permlane32_swap_b32_e32 v38, v39
	s_nop 1
	v_lshl_add_u64 v[48:49], v[214:215], 1, v[48:49]
	global_store_dwordx4 v[48:49], v[44:47], off
	global_store_dwordx4 v[48:49], v[40:43], off offset:256
	s_and_saveexec_b64 s[4:5], vcc
	s_cbranch_execz .LBB0_1133
	v_lshlrev_b64 v[36:37], 6, v[36:37]
	v_lshl_add_u64 v[36:37], s[18:19], 0, v[36:37]
	v_lshl_add_u64 v[36:37], s[44:45], 2, v[36:37]
	s_lshl_b32 s56, s53, 2
	v_lshl_add_u64 v[36:37], v[36:37], 0, s[56:57]
	s_waitcnt lgkmcnt(0)
	v_add_f32_e32 v38, v38, v39
	global_store_dword v[36:37], v38, off
.LBB0_1133:
	s_or_b64 exec, exec, s[4:5]
	v_lshlrev_b32_e32 v36, 16, v136
	v_and_b32_e32 v37, 0xffff0000, v136
	v_lshlrev_b32_e32 v38, 16, v137
	s_waitcnt lgkmcnt(0)
	v_and_b32_e32 v39, 0xffff0000, v137
	v_lshlrev_b32_e32 v40, 16, v138
	v_and_b32_e32 v41, 0xffff0000, v138
	v_lshlrev_b32_e32 v42, 16, v139
	v_and_b32_e32 v43, 0xffff0000, v139
	v_pk_add_f32 v[32:33], v[32:33], v[36:37]
	v_pk_add_f32 v[34:35], v[34:35], v[38:39]
	v_pk_add_f32 v[36:37], v[30:31], v[42:43]
	v_pk_add_f32 v[30:31], v[28:29], v[40:41]
	v_cvt_pk_bf16_f32 v28, v32, v33
	v_cvt_pk_bf16_f32 v29, v34, v35
	v_and_b32_e32 v33, 0xffff0000, v28
	v_lshlrev_b32_e32 v32, 16, v28
	v_and_b32_e32 v35, 0xffff0000, v29
	v_mul_f32_e32 v33, v33, v33
	v_cvt_pk_bf16_f32 v30, v30, v31
	v_cvt_pk_bf16_f32 v31, v36, v37
	v_lshlrev_b32_e32 v34, 16, v29
	v_fmac_f32_e32 v33, v32, v32
	v_mul_f32_e32 v32, v35, v35
	v_and_b32_e32 v37, 0xffff0000, v30
	v_and_b32_e32 v39, 0xffff0000, v31
	v_fmac_f32_e32 v32, v34, v34
	v_lshlrev_b32_e32 v36, 16, v30
	v_lshlrev_b32_e32 v38, 16, v31
	v_add_f32_e32 v32, v33, v32
	v_mul_f32_e32 v33, v37, v37
	v_mul_f32_e32 v34, v39, v39
	v_fmac_f32_e32 v33, v36, v36
	v_fmac_f32_e32 v34, v38, v38
	v_add_f32_e32 v33, v33, v34
	v_add_f32_e32 v40, v32, v33
	v_lshlrev_b32_e32 v32, 16, v128
	v_and_b32_e32 v33, 0xffff0000, v128
	v_lshlrev_b32_e32 v34, 16, v129
	v_and_b32_e32 v35, 0xffff0000, v129
	v_lshlrev_b32_e32 v36, 16, v130
	v_and_b32_e32 v37, 0xffff0000, v130
	v_pk_add_f32 v[24:25], v[24:25], v[32:33]
	v_lshlrev_b32_e32 v38, 16, v131
	v_and_b32_e32 v39, 0xffff0000, v131
	v_pk_add_f32 v[26:27], v[26:27], v[34:35]
	v_pk_add_f32 v[20:21], v[20:21], v[36:37]
	v_cvt_pk_bf16_f32 v24, v24, v25
	v_pk_add_f32 v[22:23], v[22:23], v[38:39]
	v_cvt_pk_bf16_f32 v25, v26, v27
	v_cvt_pk_bf16_f32 v26, v20, v21
	v_and_b32_e32 v21, 0xffff0000, v24
	v_cvt_pk_bf16_f32 v27, v22, v23
	v_lshlrev_b32_e32 v20, 16, v24
	v_and_b32_e32 v23, 0xffff0000, v25
	v_mul_f32_e32 v21, v21, v21
	v_lshlrev_b32_e32 v22, 16, v25
	v_fmac_f32_e32 v21, v20, v20
	v_mul_f32_e32 v20, v23, v23
	v_and_b32_e32 v33, 0xffff0000, v26
	v_and_b32_e32 v35, 0xffff0000, v27
	v_fmac_f32_e32 v20, v22, v22
	v_lshlrev_b32_e32 v32, 16, v26
	v_lshlrev_b32_e32 v34, 16, v27
	v_add_f32_e32 v20, v21, v20
	v_mul_f32_e32 v21, v33, v33
	v_mul_f32_e32 v22, v35, v35
	v_fmac_f32_e32 v21, v32, v32
	v_fmac_f32_e32 v22, v34, v34
	v_add_f32_e32 v21, v21, v22
	v_add_f32_e32 v20, v20, v21
	v_add_f32_e32 v22, v40, v20
	v_mov_b32_e32 v23, v22
	s_nop 3
	v_permlane16_swap_b32_e32 v22, v23
	s_nop 1
	v_add_u32_e32 v20, 0xa0, v216
	v_ashrrev_i32_e32 v21, 31, v20
	v_lshlrev_b64 v[32:33], 11, v[20:21]
	v_lshl_add_u64 v[32:33], s[14:15], 0, v[32:33]
	s_waitcnt lgkmcnt(0)
	v_add_f32_e32 v22, v22, v23
	v_mov_b32_e32 v23, v22
	s_nop 3
	v_permlane32_swap_b32_e32 v22, v23
	s_nop 1
	v_lshl_add_u64 v[32:33], v[214:215], 1, v[32:33]
	global_store_dwordx4 v[32:33], v[28:31], off
	global_store_dwordx4 v[32:33], v[24:27], off offset:256
	s_and_saveexec_b64 s[4:5], vcc
	s_cbranch_execz .LBB0_1135
	v_lshlrev_b64 v[20:21], 6, v[20:21]
	v_lshl_add_u64 v[20:21], s[18:19], 0, v[20:21]
	v_lshl_add_u64 v[20:21], s[44:45], 2, v[20:21]
	s_lshl_b32 s56, s53, 2
	v_lshl_add_u64 v[20:21], v[20:21], 0, s[56:57]
	s_waitcnt lgkmcnt(0)
	v_add_f32_e32 v22, v22, v23
	global_store_dword v[20:21], v22, off
.LBB0_1135:
	s_or_b64 exec, exec, s[4:5]
	v_lshlrev_b32_e32 v20, 16, v116
	v_and_b32_e32 v21, 0xffff0000, v116
	v_lshlrev_b32_e32 v22, 16, v117
	s_waitcnt lgkmcnt(0)
	v_and_b32_e32 v23, 0xffff0000, v117
	v_lshlrev_b32_e32 v24, 16, v118
	v_and_b32_e32 v25, 0xffff0000, v118
	v_lshlrev_b32_e32 v26, 16, v119
	v_and_b32_e32 v27, 0xffff0000, v119
	v_pk_add_f32 v[16:17], v[16:17], v[20:21]
	v_pk_add_f32 v[18:19], v[18:19], v[22:23]
	v_pk_add_f32 v[20:21], v[14:15], v[26:27]
	v_pk_add_f32 v[14:15], v[12:13], v[24:25]
	v_cvt_pk_bf16_f32 v12, v16, v17
	v_cvt_pk_bf16_f32 v13, v18, v19
	v_and_b32_e32 v17, 0xffff0000, v12
	v_lshlrev_b32_e32 v16, 16, v12
	v_and_b32_e32 v19, 0xffff0000, v13
	v_mul_f32_e32 v17, v17, v17
	v_cvt_pk_bf16_f32 v14, v14, v15
	v_cvt_pk_bf16_f32 v15, v20, v21
	v_lshlrev_b32_e32 v18, 16, v13
	v_fmac_f32_e32 v17, v16, v16
	v_mul_f32_e32 v16, v19, v19
	v_and_b32_e32 v21, 0xffff0000, v14
	v_and_b32_e32 v23, 0xffff0000, v15
	v_fmac_f32_e32 v16, v18, v18
	v_lshlrev_b32_e32 v20, 16, v14
	v_lshlrev_b32_e32 v22, 16, v15
	v_add_f32_e32 v16, v17, v16
	v_mul_f32_e32 v17, v21, v21
	v_mul_f32_e32 v18, v23, v23
	v_fmac_f32_e32 v17, v20, v20
	v_fmac_f32_e32 v18, v22, v22
	v_add_f32_e32 v17, v17, v18
	v_add_f32_e32 v24, v16, v17
	v_lshlrev_b32_e32 v16, 16, v108
	v_and_b32_e32 v17, 0xffff0000, v108
	v_lshlrev_b32_e32 v18, 16, v109
	v_and_b32_e32 v19, 0xffff0000, v109
	v_lshlrev_b32_e32 v20, 16, v110
	v_and_b32_e32 v21, 0xffff0000, v110
	v_pk_add_f32 v[8:9], v[8:9], v[16:17]
	v_lshlrev_b32_e32 v22, 16, v111
	v_and_b32_e32 v23, 0xffff0000, v111
	v_pk_add_f32 v[10:11], v[10:11], v[18:19]
	v_pk_add_f32 v[4:5], v[4:5], v[20:21]
	v_cvt_pk_bf16_f32 v8, v8, v9
	v_pk_add_f32 v[6:7], v[6:7], v[22:23]
	v_cvt_pk_bf16_f32 v9, v10, v11
	v_cvt_pk_bf16_f32 v10, v4, v5
	v_and_b32_e32 v5, 0xffff0000, v8
	v_cvt_pk_bf16_f32 v11, v6, v7
	v_lshlrev_b32_e32 v4, 16, v8
	v_and_b32_e32 v7, 0xffff0000, v9
	v_mul_f32_e32 v5, v5, v5
	v_lshlrev_b32_e32 v6, 16, v9
	v_fmac_f32_e32 v5, v4, v4
	v_mul_f32_e32 v4, v7, v7
	v_and_b32_e32 v17, 0xffff0000, v10
	v_and_b32_e32 v19, 0xffff0000, v11
	v_fmac_f32_e32 v4, v6, v6
	v_lshlrev_b32_e32 v16, 16, v10
	v_lshlrev_b32_e32 v18, 16, v11
	v_add_f32_e32 v4, v5, v4
	v_mul_f32_e32 v5, v17, v17
	v_mul_f32_e32 v6, v19, v19
	v_fmac_f32_e32 v5, v16, v16
	v_fmac_f32_e32 v6, v18, v18
	v_add_f32_e32 v5, v5, v6
	v_add_f32_e32 v4, v4, v5
	v_add_f32_e32 v6, v24, v4
	v_mov_b32_e32 v7, v6
	s_nop 3
	v_permlane16_swap_b32_e32 v6, v7
	s_nop 1
	v_add_u32_e32 v4, 0xb0, v216
	v_ashrrev_i32_e32 v5, 31, v4
	v_lshlrev_b64 v[16:17], 11, v[4:5]
	v_lshl_add_u64 v[16:17], s[14:15], 0, v[16:17]
	s_waitcnt lgkmcnt(0)
	v_add_f32_e32 v6, v6, v7
	v_mov_b32_e32 v7, v6
	s_nop 3
	v_permlane32_swap_b32_e32 v6, v7
	s_nop 1
	v_lshl_add_u64 v[16:17], v[214:215], 1, v[16:17]
	global_store_dwordx4 v[16:17], v[12:15], off
	global_store_dwordx4 v[16:17], v[8:11], off offset:256
	s_and_saveexec_b64 s[4:5], vcc
	s_cbranch_execz .LBB0_1137
	v_lshlrev_b64 v[4:5], 6, v[4:5]
	v_lshl_add_u64 v[4:5], s[18:19], 0, v[4:5]
	v_lshl_add_u64 v[4:5], s[44:45], 2, v[4:5]
	s_lshl_b32 s56, s53, 2
	v_lshl_add_u64 v[4:5], v[4:5], 0, s[56:57]
	s_waitcnt lgkmcnt(0)
	v_add_f32_e32 v6, v6, v7
	global_store_dword v[4:5], v6, off
